# skip the no-op conversion flush calls at the end of P7 and P8 when the workgroup's items are already done
# speedup vs baseline: 1.0140x; 1.0013x over previous
.LBB0_845:
	v_readlane_b32 vcc_lo, v255, 2
	s_nop 3
	s_cmp_ge_u32 vcc_lo, 32
	s_cbranch_scc1 .Lmy_ret_gu8
	v_writelane_b32 v255, 8, 5
	v_writelane_b32 v255, 64, 6
	s_branch .Lmy_cvgu

.LBB0_1147:
	s_load_dwordx2 s[88:89], s[0:1], 0xb8
	v_readlane_b32 s87, v252, 8
	v_readlane_b32 vcc_lo, v255, 3
	s_nop 3
	s_cmp_ge_u32 vcc_lo, 16
	s_cbranch_scc1 .Lmy_ret_dn3
	v_writelane_b32 v255, 3, 5
	v_writelane_b32 v255, 64, 6
